# GLA MFMA group: workgroup barrier B (needed only by the preparation waves) moved from the end of the output block to after its second strip, so both wave groups have balanced segments
# speedup vs baseline: 1.0052x; 1.0004x over previous
; #define LAS __attribute__((address_space(3)))
; __device__ __forceinline__ void lds_barrier() { asm volatile("s_waitcnt lgkmcnt(0)" ::: "memory"); __builtin_amdgcn_s_barrier(); asm volatile("" ::: "memory"); }
; __device__ __forceinline__ void gla_fast_unit(int unit, const bf16_t* P, const float* w_up, const float* b_up, float* Of, float* Ob, LAS unsigned char* lds0) {
;     ...
;     if (wv < 4) {
;         const int mw = wv;
;         const unsigned ooff = (unsigned)((dir ? 63 - l15 : l15) * 2048 + (h * 128 + 32 * mw + 4 * q) * 2);
;         f32x4 S[4][2];
; #pragma unroll
;         for (int dt = 0; dt < 4; ++dt) { S[dt][0] = (f32x4){0.f, 0.f, 0.f, 0.f}; S[dt][1] = (f32x4){0.f, 0.f, 0.f, 0.f}; }
;         for (int cidx = -1; cidx < NCH + 1; ++cidx) {
;             LAS unsigned char* lds = lds0 + (cidx & 1) * G_END;
;     ...
;             lds_barrier();
;             if (cidx >= 0 && cidx < NCH) {
; #pragma unroll
;                 for (int dt = 0; dt < 4; ++dt) { const f32x4 dec = *(const LAS f32x4*)(lds + G_BEND + (16 * dt + 4 * q) * 4); S[dt][0] = S[dt][0] * dec; S[dt][1] = S[dt][1] * dec; }
; #pragma unroll
;                 for (int kk = 0; kk < 2; ++kk) { bf16x8 vs[2];
; #pragma unroll
;                     for (int et = 0; et < 2; ++et) vs[et] = tr_frag(lds + G_VS + (32 * kk + 8 * q + trq) * G_RSV + (32 * mw + 16 * et + 4 * trp) * 2, 4 * G_RSV);
; #pragma unroll
;                     for (int dt = 0; dt < 4; ++dt) { const bf16x8 ktf = tr_frag(lds + G_KP + (32 * kk + 8 * q + trq) * G_RS + (16 * dt + 4 * trp) * 2, 4 * G_RS);
;                         S[dt][0] = __builtin_amdgcn_mfma_f32_16x16x32_bf16(ktf, vs[0], S[dt][0], 0, 0, 0); S[dt][1] = __builtin_amdgcn_mfma_f32_16x16x32_bf16(ktf, vs[1], S[dt][1], 0, 0, 0); } }
;             }
.LBB0_1199:
	s_and_b64 vcc, exec, s[2:3]
	s_cbranch_vccz .LBB0_1205
	v_lshlrev_b32_e32 v2, 11, v1
	v_readlane_b32 s6, v254, 63
	v_readlane_b32 s8, v255, 1
	v_xor_b32_e32 v3, 0x1f800, v2
	s_and_b64 s[2:3], s[4:5], exec
	v_readlane_b32 s7, v255, 0
	v_readlane_b32 s9, v255, 2
	v_cndmask_b32_e64 v2, v3, v2, s[4:5]
	s_movk_i32 s12, 0x120
	s_mov_b32 s13, 0x8000
	s_mov_b32 s14, 0x10000
	s_mov_b32 s15, 0x18000
	v_or_b32_e32 v3, v175, v182
	v_mov_b32_e32 v4, 0x2400
	s_cselect_b32 s2, s7, s9
	s_cselect_b32 s3, s6, s8
	s_cselect_b32 s13, s13, 0xffff8000
	s_cselect_b32 s14, s14, 0xffff0000
	s_cselect_b32 s15, s15, 0xfffe8000
	v_mad_u32_u24 v70, v3, s12, v4
	s_lshl_b32 s12, s34, 5
	s_or_b32 s12, s31, s12
	s_waitcnt lgkmcnt(0)
	s_barrier
	v_mul_u32_u24_e32 v68, 0x120, v3
	v_mul_u32_u24_e32 v69, 0xa0, v3
	v_or_b32_e32 v3, s12, v169
	s_waitcnt lgkmcnt(0)
	s_barrier
	v_lshl_or_b32 v58, v3, 1, v2
	v_mov_b32_e32 v4, 0
	v_mul_u32_u24_e32 v66, 0xa0, v1
	v_mul_u32_u24_e32 v67, 0x120, v173
	v_cmp_gt_u32_e32 vcc, v179, v1
	v_cmp_gt_u32_e64 s[6:7], v180, v1
	v_cmp_lt_u32_e64 s[8:9], v169, v1
	v_cmp_gt_u32_e64 s[10:11], v169, v1
	s_and_b32 s12, s30, 0xc0
	v_mov_b32_e32 v59, v4
	v_add_u32_e32 v60, s13, v58
	v_mov_b32_e32 v61, v4
	v_add_u32_e32 v62, s14, v58
	v_mov_b32_e32 v63, v4
	v_add_u32_e32 v64, s15, v58
	v_mov_b32_e32 v65, v4
	s_mov_b32 s13, 0
	s_movk_i32 s14, 0xff00
	s_movk_i32 s15, 0x10c0
	s_mov_b32 s16, 0
	v_mov_b32_e32 v34, v4
	s_waitcnt vmcnt(35)
	v_mov_b32_e32 v35, v4
	v_mov_b32_e32 v36, v4
	v_mov_b32_e32 v37, v4
	v_mov_b32_e32 v6, v4
	v_mov_b32_e32 v7, v4
	v_mov_b32_e32 v8, v4
	v_mov_b32_e32 v9, v4
	v_mov_b32_e32 v10, v4
	v_mov_b32_e32 v11, v4
	v_mov_b32_e32 v12, v4
	v_mov_b32_e32 v13, v4
	v_mov_b32_e32 v14, v4
	v_mov_b32_e32 v15, v4
	v_mov_b32_e32 v16, v4
	v_mov_b32_e32 v17, v4
	v_mov_b32_e32 v18, v4
	v_mov_b32_e32 v19, v4
	v_mov_b32_e32 v20, v4
	v_mov_b32_e32 v21, v4
	v_mov_b32_e32 v22, v4
	v_mov_b32_e32 v23, v4
	v_mov_b32_e32 v24, v4
	v_mov_b32_e32 v25, v4
	v_mov_b32_e32 v26, v4
	v_mov_b32_e32 v27, v4
	v_mov_b32_e32 v28, v4
	v_mov_b32_e32 v29, v4
	v_mov_b32_e32 v30, v4
	v_mov_b32_e32 v31, v4
	v_mov_b32_e32 v32, v4
	v_mov_b32_e32 v33, v4
	s_waitcnt vmcnt(0)
	s_branch .LBB0_1202
.LBB0_1201:
	s_waitcnt lgkmcnt(0)
	s_barrier
.Lgla_upd:
	v_add_u32_e32 v2, s17, v176
	v_add_u32_e32 v2, 0x11800, v2
	s_nop 0
	ds_read_b128 v[38:41], v2
	ds_read_b128 v[42:45], v2 offset:64
	v_add_u32_e32 v3, s17, v178
	v_add_u32_e32 v71, v3, v69
	v_add3_u32 v5, v3, v68, s12
	s_waitcnt lgkmcnt(1)
	v_pk_mul_f32 v[34:35], v[34:35], v[38:39]
	v_pk_mul_f32 v[36:37], v[36:37], v[40:41]
	ds_read_b64_tr_b16 v[48:49], v71 offset:21120
	ds_read_b64_tr_b16 v[46:47], v71 offset:20480
	ds_read_b64_tr_b16 v[52:53], v5 offset:31872
	ds_read_b64_tr_b16 v[50:51], v5 offset:30720
	ds_read_b64_tr_b16 v[56:57], v5 offset:31904
	ds_read_b64_tr_b16 v[54:55], v5 offset:30752
	ds_read_b64_tr_b16 v[72:73], v71 offset:20512
	ds_read_b64_tr_b16 v[76:77], v71 offset:20544
	ds_read_b64_tr_b16 v[80:81], v71 offset:20576
	ds_read_b64_tr_b16 v[74:75], v71 offset:21152
	ds_read_b64_tr_b16 v[78:79], v71 offset:21184
	ds_read_b64_tr_b16 v[82:83], v71 offset:21216
	v_pk_mul_f32 v[6:7], v[6:7], v[38:39]
	v_pk_mul_f32 v[8:9], v[8:9], v[40:41]
	s_waitcnt lgkmcnt(12)
	v_pk_mul_f32 v[10:11], v[10:11], v[42:43]
	v_pk_mul_f32 v[12:13], v[12:13], v[44:45]
	ds_read_b128 v[38:41], v2 offset:128
	v_pk_mul_f32 v[14:15], v[14:15], v[42:43]
	v_pk_mul_f32 v[16:17], v[16:17], v[44:45]
	ds_read_b128 v[42:45], v2 offset:192
	s_waitcnt lgkmcnt(10)
	v_mfma_f32_16x16x32_bf16 v[34:37], v[46:49], v[50:53], v[34:37]
	s_waitcnt lgkmcnt(1)
	v_pk_mul_f32 v[18:19], v[18:19], v[38:39]
	v_pk_mul_f32 v[20:21], v[20:21], v[40:41]
	v_pk_mul_f32 v[22:23], v[22:23], v[38:39]
	v_pk_mul_f32 v[24:25], v[24:25], v[40:41]
	s_waitcnt lgkmcnt(0)
	v_pk_mul_f32 v[26:27], v[26:27], v[42:43]
	v_pk_mul_f32 v[28:29], v[28:29], v[44:45]
	v_pk_mul_f32 v[30:31], v[30:31], v[42:43]
	v_pk_mul_f32 v[32:33], v[32:33], v[44:45]
	v_mfma_f32_16x16x32_bf16 v[6:9], v[46:49], v[54:57], v[6:9]
	v_add3_u32 v2, v3, v70, s12
	s_add_i32 s16, s16, 1
	s_add_i32 s14, s14, 64
	v_mfma_f32_16x16x32_bf16 v[10:13], v[72:75], v[50:53], v[10:13]
	s_sub_i32 s15, s15, 64
	s_cmpk_eq_i32 s15, 0xffc0
	v_mfma_f32_16x16x32_bf16 v[14:17], v[72:75], v[54:57], v[14:17]
	v_mfma_f32_16x16x32_bf16 v[18:21], v[76:79], v[50:53], v[18:21]
	v_mfma_f32_16x16x32_bf16 v[22:25], v[76:79], v[54:57], v[22:25]
	v_mfma_f32_16x16x32_bf16 v[26:29], v[80:83], v[50:53], v[26:29]
	v_mfma_f32_16x16x32_bf16 v[30:33], v[80:83], v[54:57], v[30:33]
	ds_read_b64_tr_b16 v[38:39], v71 offset:25600
	ds_read_b64_tr_b16 v[40:41], v71 offset:26240
	ds_read_b64_tr_b16 v[44:45], v2 offset:31872
	ds_read_b64_tr_b16 v[42:43], v2 offset:30720
	ds_read_b64_tr_b16 v[48:49], v2 offset:31904
	ds_read_b64_tr_b16 v[46:47], v2 offset:30752
	ds_read_b64_tr_b16 v[50:51], v71 offset:25632
	ds_read_b64_tr_b16 v[54:55], v71 offset:25664
	ds_read_b64_tr_b16 v[72:73], v71 offset:25696
	ds_read_b64_tr_b16 v[52:53], v71 offset:26272
	ds_read_b64_tr_b16 v[56:57], v71 offset:26304
	ds_read_b64_tr_b16 v[74:75], v71 offset:26336
	s_waitcnt lgkmcnt(8)
	v_mfma_f32_16x16x32_bf16 v[34:37], v[38:41], v[42:45], v[34:37]
	s_waitcnt lgkmcnt(6)
	v_mfma_f32_16x16x32_bf16 v[6:9], v[38:41], v[46:49], v[6:9]
	s_waitcnt lgkmcnt(2)
	v_mfma_f32_16x16x32_bf16 v[10:13], v[50:53], v[42:45], v[10:13]
	v_mfma_f32_16x16x32_bf16 v[14:17], v[50:53], v[46:49], v[14:17]
	s_waitcnt lgkmcnt(1)
	v_mfma_f32_16x16x32_bf16 v[18:21], v[54:57], v[42:45], v[18:21]
	v_mfma_f32_16x16x32_bf16 v[22:25], v[54:57], v[46:49], v[22:25]
	s_waitcnt lgkmcnt(0)
	v_mfma_f32_16x16x32_bf16 v[26:29], v[72:75], v[42:45], v[26:29]
	v_mfma_f32_16x16x32_bf16 v[30:33], v[72:75], v[46:49], v[30:33]
	s_cbranch_scc1 .LBB0_1204
; __device__ __forceinline__ void gla_fast_unit(int unit, const bf16_t* P, const float* w_up, const float* b_up, float* Of, float* Ob, LAS unsigned char* lds0) {
;     ...
;             if (cidx >= CL / 64 && cidx < NCH) {
;                 bf16x8 sfr[2][2];
; #pragma unroll
;                 for (int kk = 0; kk < 2; ++kk)
; #pragma unroll
;                     for (int et = 0; et < 2; ++et) { const u32x4 w = (u32x4){pk2(S[2 * kk][et][0], S[2 * kk][et][1]), pk2(S[2 * kk][et][2], S[2 * kk][et][3]), pk2(S[2 * kk + 1][et][0], S[2 * kk + 1][et][1]), pk2(S[2 * kk + 1][et][2], S[2 * kk + 1][et][3])};
;                         sfr[kk][et] = __builtin_bit_cast(bf16x8, w); }
;                 bf16x8 kf[4][2];
; #pragma unroll
;                 for (int st = 0; st < 4; ++st)
; #pragma unroll
;                     for (int kk = 0; kk < 2; ++kk) { const LAS unsigned char* kp = lds + G_KS + (16 * st + l15) * G_RS + (32 * kk + 4 * q) * 2;
;                         const u32x2 a0 = *(const LAS u32x2*)kp, a1 = *(const LAS u32x2*)(kp + 32); kf[st][kk] = __builtin_bit_cast(bf16x8, (u32x4){a0.x, a0.y, a1.x, a1.y}); }
;                 bf16x8 vfo[2][2];
; #pragma unroll
;                 for (int m = 0; m < 2; ++m)
; #pragma unroll
;                     for (int et = 0; et < 2; ++et) vfo[m][et] = tr_frag(lds + G_VS + (32 * m + 4 * q + trq) * G_RSV + (32 * mw + 16 * et + 4 * trp) * 2, 16 * G_RSV);
; #pragma unroll
;                 for (int sg = 0; sg < 4; ++sg) {
;                     bf16x8 qf[2];
; #pragma unroll
;                     for (int kk = 0; kk < 2; ++kk) { const LAS unsigned char* qp = lds + G_QS + (16 * sg + l15) * G_RS + (32 * kk + 4 * q) * 2;
;                         const u32x2 a0 = *(const LAS u32x2*)qp, a1 = *(const LAS u32x2*)(qp + 32); qf[kk] = __builtin_bit_cast(bf16x8, (u32x4){a0.x, a0.y, a1.x, a1.y}); }
;                     f32x4 accO[2] = {(f32x4){0.f, 0.f, 0.f, 0.f}, (f32x4){0.f, 0.f, 0.f, 0.f}};
; #pragma unroll
;                     for (int kk = 0; kk < 2; ++kk)
; #pragma unroll
;                         for (int et = 0; et < 2; ++et) accO[et] = __builtin_amdgcn_mfma_f32_16x16x32_bf16(sfr[kk][et], qf[kk], accO[et], 0, 0, 0);
; #pragma unroll
;                     for (int m = 0; m <= (sg >> 1); ++m) {
;                         unsigned pk[4];
; #pragma unroll
;                         for (int hf = 0; hf < 2; ++hf) { const int st = 2 * m + hf;
.LBB0_1202:
	s_bitcmp1_b32 s16, 0
	s_cselect_b32 s17, 0x11900, 0
	s_waitcnt lgkmcnt(0)
	s_barrier
	s_add_i32 s17, s17, 0
	s_cmp_lt_u32 s16, 4
	s_cbranch_scc1 .LBB0_1201
	v_add3_u32 v71, s17, v175, v66
	v_add_u32_e32 v2, 0x2800, v71
	ds_read2_b64 v[88:91], v2 offset1:4
	v_cvt_pk_bf16_f32 v38, v34, v35
	v_cvt_pk_bf16_f32 v39, v36, v37
	v_cvt_pk_bf16_f32 v40, v10, v11
	v_cvt_pk_bf16_f32 v41, v12, v13
	v_cvt_pk_bf16_f32 v42, v6, v7
	v_cvt_pk_bf16_f32 v43, v8, v9
	v_cvt_pk_bf16_f32 v44, v14, v15
	v_cvt_pk_bf16_f32 v45, v16, v17
	ds_read2_b64 v[72:75], v71 offset1:4
	ds_read2_b64 v[96:99], v2 offset0:8 offset1:12
	ds_read2_b64 v[80:83], v71 offset0:8 offset1:12
	s_waitcnt lgkmcnt(2)
	v_mfma_f32_16x16x32_bf16 v[50:53], v[38:41], v[72:75], 0
	v_cvt_pk_bf16_f32 v46, v18, v19
	v_cvt_pk_bf16_f32 v47, v20, v21
	v_cvt_pk_bf16_f32 v48, v26, v27
	v_mfma_f32_16x16x32_bf16 v[54:57], v[42:45], v[72:75], 0
	v_cvt_pk_bf16_f32 v49, v28, v29
	v_cvt_pk_bf16_f32 v76, v22, v23
	v_cvt_pk_bf16_f32 v77, v24, v25
	v_mfma_f32_16x16x32_bf16 v[72:75], v[88:91], v[72:75], 0
	v_cvt_pk_bf16_f32 v78, v30, v31
	v_cvt_pk_bf16_f32 v79, v32, v33
	v_add_u32_e32 v2, s17, v67
	s_waitcnt lgkmcnt(0)
	v_mfma_f32_16x16x32_bf16 v[72:75], v[96:99], v[80:83], v[72:75]
	v_add3_u32 v84, v2, v178, s12
	v_mov_b32_e32 v2, s13
	s_and_b64 s[18:19], s[4:5], exec
	v_mfma_f32_16x16x32_bf16 v[92:95], v[46:49], v[80:83], v[50:53]
	s_cselect_b32 s18, s14, s15
	s_nop 2
	v_cndmask_b32_e64 v2, v72, v2, s[10:11]
	v_cndmask_b32_e64 v2, v2, v72, s[8:9]
	v_mfma_f32_16x16x32_bf16 v[100:103], v[76:79], v[80:83], v[54:57]
	ds_read_b64_tr_b16 v[106:107], v84 offset:35328
	ds_read_b64_tr_b16 v[110:111], v84 offset:35360
	s_nop 0
	ds_read_b64_tr_b16 v[54:55], v84 offset:39936
	ds_read_b64_tr_b16 v[50:51], v84 offset:39968
	ds_read_b64_tr_b16 v[104:105], v84 offset:30720
	ds_read_b64_tr_b16 v[108:109], v84 offset:30752
	ds_read_b64_tr_b16 v[52:53], v84 offset:44576
	v_cndmask_b32_e64 v3, 0, v73, s[8:9]
	v_cndmask_b32_e64 v5, v74, 0, s[6:7]
	v_cndmask_b32_e64 v56, v75, 0, vcc
	v_cvt_pk_bf16_f32 v2, v2, v3
	v_cvt_pk_bf16_f32 v3, v5, v56
	v_mov_b32_e32 v5, v4
	s_add_i32 s18, s18, s24
	s_ashr_i32 s19, s18, 31
	s_waitcnt lgkmcnt(2)
	v_mfma_f32_16x16x32_bf16 v[72:75], v[104:107], v[2:5], v[92:95]
	s_lshl_b64 s[18:19], s[18:19], 11
	s_add_u32 s18, s3, s18
	s_addc_u32 s19, s2, s19
	s_waitcnt lgkmcnt(1)
	v_mfma_f32_16x16x32_bf16 v[80:83], v[108:111], v[2:5], v[100:103]
	v_add_u32_e32 v2, 0x800, v71
	ds_read2_b64 v[92:95], v2 offset0:64 offset1:68
	ds_read2_b64 v[116:119], v2 offset0:72 offset1:76
	v_add_u32_e32 v2, 0x3000, v71
	ds_read2_b64 v[124:127], v2 offset0:64 offset1:68
	ds_read2_b64 v[128:131], v2 offset0:72 offset1:76
	s_waitcnt lgkmcnt(3)
	v_mfma_f32_16x16x32_bf16 v[100:103], v[38:41], v[92:95], 0
	v_mov_b32_e32 v2, s13
	v_mfma_f32_16x16x32_bf16 v[112:115], v[42:45], v[92:95], 0
	v_mfma_f32_16x16x32_bf16 v[120:123], v[88:91], v[92:95], 0
	s_waitcnt lgkmcnt(1)
	v_mfma_f32_16x16x32_bf16 v[92:95], v[124:127], v[92:95], 0
	s_waitcnt lgkmcnt(0)
	v_mfma_f32_16x16x32_bf16 v[92:95], v[128:131], v[116:119], v[92:95]
	v_mfma_f32_16x16x32_bf16 v[120:123], v[96:99], v[116:119], v[120:123]
	v_mfma_f32_16x16x32_bf16 v[100:103], v[46:49], v[116:119], v[100:103]
	s_nop 5
	v_cndmask_b32_e64 v2, v92, v2, s[10:11]
	v_cndmask_b32_e64 v2, v2, v92, s[8:9]
	v_cndmask_b32_e64 v3, 0, v93, s[8:9]
	v_mfma_f32_16x16x32_bf16 v[112:115], v[76:79], v[116:119], v[112:115]
	v_cndmask_b32_e64 v5, v94, 0, s[6:7]
	v_cndmask_b32_e64 v56, v95, 0, vcc
	v_cvt_pk_bf16_f32 v120, v120, v121
	v_cvt_pk_bf16_f32 v121, v122, v123
	v_cvt_pk_bf16_f32 v122, v2, v3
	v_cvt_pk_bf16_f32 v123, v5, v56
	v_add_u32_e32 v2, 0x1000, v71
	ds_read2_b64 v[132:135], v2 offset0:136 offset1:140
	v_mfma_f32_16x16x32_bf16 v[92:95], v[104:107], v[120:123], v[100:103]
	v_mfma_f32_16x16x32_bf16 v[100:103], v[108:111], v[120:123], v[112:115]
	s_barrier
; __device__ __forceinline__ void gla_fast_unit(int unit, const bf16_t* P, const float* w_up, const float* b_up, float* Of, float* Ob, LAS unsigned char* lds0) {
;     ...
;                 for (int sg = 0; sg < 4; ++sg) {
;                     bf16x8 qf[2];
; #pragma unroll
;                     for (int kk = 0; kk < 2; ++kk) { const LAS unsigned char* qp = lds + G_QS + (16 * sg + l15) * G_RS + (32 * kk + 4 * q) * 2;
;                         const u32x2 a0 = *(const LAS u32x2*)qp, a1 = *(const LAS u32x2*)(qp + 32); qf[kk] = __builtin_bit_cast(bf16x8, (u32x4){a0.x, a0.y, a1.x, a1.y}); }
;                     f32x4 accO[2] = {(f32x4){0.f, 0.f, 0.f, 0.f}, (f32x4){0.f, 0.f, 0.f, 0.f}};
; #pragma unroll
;                     for (int kk = 0; kk < 2; ++kk)
; #pragma unroll
;                         for (int et = 0; et < 2; ++et) accO[et] = __builtin_amdgcn_mfma_f32_16x16x32_bf16(sfr[kk][et], qf[kk], accO[et], 0, 0, 0);
; #pragma unroll
;                     for (int m = 0; m <= (sg >> 1); ++m) {
;                         unsigned pk[4];
; #pragma unroll
;                         for (int hf = 0; hf < 2; ++hf) { const int st = 2 * m + hf;
;                             if (st <= sg) { f32x4 X = (f32x4){0.f, 0.f, 0.f, 0.f};
; #pragma unroll
;                                 for (int kk = 0; kk < 2; ++kk) X = __builtin_amdgcn_mfma_f32_16x16x32_bf16(kf[st][kk], qf[kk], X, 0, 0, 0);
;                                 if (st == sg) {
; #pragma unroll
;                                     for (int r = 0; r < 4; ++r) if (4 * q + r > l15) X[r] = 0.f; }
;                                 pk[2 * hf] = pk2(X[0], X[1]); pk[2 * hf + 1] = pk2(X[2], X[3]); }
;                             else { pk[2 * hf] = 0u; pk[2 * hf + 1] = 0u; } }
;                         const bf16x8 pa = __builtin_bit_cast(bf16x8, (u32x4){pk[0], pk[1], pk[2], pk[3]});
; #pragma unroll
;                         for (int et = 0; et < 2; ++et) accO[et] = __builtin_amdgcn_mfma_f32_16x16x32_bf16(vfo[m][et], pa, accO[et], 0, 0, 0);
;                     }
;                     { char* ob = (char*)O + (size_t)gla_lowrow(b, dir, cidx * 64) * 2048 + (ooff + (unsigned)((dir ? -sg : sg) * 16 * 2048));
; #pragma unroll
;                         for (int et = 0; et < 2; ++et) { u32x2 w; w.x = pk2(accO[et][0], accO[et][1]); w.y = pk2(accO[et][2], accO[et][3]); *(u32x2*)(ob + 32 * et) = w; } }
;                 }
	s_nop 1
	ds_read2_b64 v[112:115], v2 offset0:128 offset1:132
	v_add_u32_e32 v2, 0x3800, v71
	ds_read2_b64 v[144:147], v2 offset0:128 offset1:132
	ds_read2_b64 v[148:151], v2 offset0:136 offset1:140
	s_waitcnt lgkmcnt(2)
	v_mfma_f32_16x16x32_bf16 v[136:139], v[88:91], v[112:115], 0
	ds_read_b64_tr_b16 v[56:57], v84 offset:44544
	v_add_u32_e32 v84, 0x4000, v71
	v_add_u32_e32 v71, 0x1800, v71
	v_mfma_f32_16x16x32_bf16 v[140:143], v[124:127], v[112:115], 0
	v_mov_b32_e32 v2, s13
	v_mfma_f32_16x16x32_bf16 v[116:119], v[38:41], v[112:115], 0
	v_mfma_f32_16x16x32_bf16 v[120:123], v[42:45], v[112:115], 0
	s_waitcnt lgkmcnt(2)
	v_mfma_f32_16x16x32_bf16 v[112:115], v[144:147], v[112:115], 0
	v_mfma_f32_16x16x32_bf16 v[136:139], v[96:99], v[132:135], v[136:139]
	v_mfma_f32_16x16x32_bf16 v[140:143], v[128:131], v[132:135], v[140:143]
	v_mfma_f32_16x16x32_bf16 v[116:119], v[46:49], v[132:135], v[116:119]
	s_nop 5
	v_cvt_pk_bf16_f32 v136, v136, v137
	v_cvt_pk_bf16_f32 v137, v138, v139
	v_cvt_pk_bf16_f32 v138, v140, v141
	v_mfma_f32_16x16x32_bf16 v[120:123], v[76:79], v[132:135], v[120:123]
	v_cvt_pk_bf16_f32 v139, v142, v143
	ds_read2_b64 v[140:143], v71 offset0:200 offset1:204
	s_waitcnt lgkmcnt(2)
	v_mfma_f32_16x16x32_bf16 v[112:115], v[148:151], v[132:135], v[112:115]
	ds_read2_b64 v[132:135], v71 offset0:192 offset1:196
	v_mfma_f32_16x16x32_bf16 v[116:119], v[104:107], v[136:139], v[116:119]
	s_waitcnt lgkmcnt(0)
	v_mfma_f32_16x16x32_bf16 v[38:41], v[38:41], v[132:135], 0
	s_nop 3
	v_cndmask_b32_e64 v2, v112, v2, s[10:11]
	v_cndmask_b32_e64 v2, v2, v112, s[8:9]
	v_cndmask_b32_e64 v3, 0, v113, s[8:9]
	v_cndmask_b32_e64 v5, v114, 0, s[6:7]
	v_cndmask_b32_e64 v85, v115, 0, vcc
	v_mfma_f32_16x16x32_bf16 v[112:115], v[108:111], v[136:139], v[120:123]
	v_cvt_pk_bf16_f32 v2, v2, v3
	v_cvt_pk_bf16_f32 v3, v5, v85
	v_mov_b32_e32 v5, v4
	v_mfma_f32_16x16x32_bf16 v[42:45], v[42:45], v[132:135], 0
	ds_read2_b64 v[120:123], v84 offset0:192 offset1:196
	ds_read2_b64 v[136:139], v84 offset0:200 offset1:204
	v_mfma_f32_16x16x32_bf16 v[116:119], v[54:57], v[2:5], v[116:119]
	v_mfma_f32_16x16x32_bf16 v[112:115], v[50:53], v[2:5], v[112:115]
	v_lshl_add_u64 v[2:3], s[18:19], 0, v[58:59]
	v_mfma_f32_16x16x32_bf16 v[38:41], v[46:49], v[140:143], v[38:41]
	v_cvt_pk_bf16_f32 v46, v72, v73
	v_cvt_pk_bf16_f32 v47, v74, v75
	v_cvt_pk_bf16_f32 v72, v80, v81
	v_cvt_pk_bf16_f32 v73, v82, v83
	v_mfma_f32_16x16x32_bf16 v[42:45], v[76:79], v[140:143], v[42:45]
	global_store_dwordx2 v[2:3], v[46:47], off
	global_store_dwordx2 v[2:3], v[72:73], off offset:32
	v_lshl_add_u64 v[2:3], s[18:19], 0, v[60:61]
	v_cvt_pk_bf16_f32 v72, v92, v93
	v_cvt_pk_bf16_f32 v73, v94, v95
	v_cvt_pk_bf16_f32 v76, v100, v101
	v_cvt_pk_bf16_f32 v77, v102, v103
	global_store_dwordx2 v[2:3], v[72:73], off
	global_store_dwordx2 v[2:3], v[76:77], off offset:32
	v_lshl_add_u64 v[2:3], s[18:19], 0, v[62:63]
	v_cvt_pk_bf16_f32 v76, v116, v117
	v_cvt_pk_bf16_f32 v77, v118, v119
	v_mfma_f32_16x16x32_bf16 v[46:49], v[88:91], v[132:135], 0
	global_store_dwordx2 v[2:3], v[76:77], off
	v_cvt_pk_bf16_f32 v80, v112, v113
	v_cvt_pk_bf16_f32 v81, v114, v115
	v_mfma_f32_16x16x32_bf16 v[72:75], v[124:127], v[132:135], 0
	global_store_dwordx2 v[2:3], v[80:81], off offset:32
	v_mov_b32_e32 v2, s13
	v_mfma_f32_16x16x32_bf16 v[76:79], v[144:147], v[132:135], 0
	v_mfma_f32_16x16x32_bf16 v[46:49], v[96:99], v[140:143], v[46:49]
	v_mfma_f32_16x16x32_bf16 v[72:75], v[128:131], v[140:143], v[72:75]
	v_mfma_f32_16x16x32_bf16 v[76:79], v[148:151], v[140:143], v[76:79]
	s_nop 5
	v_cvt_pk_bf16_f32 v46, v46, v47
	v_cvt_pk_bf16_f32 v47, v48, v49
	v_cvt_pk_bf16_f32 v48, v72, v73
	s_waitcnt lgkmcnt(1)
	v_mfma_f32_16x16x32_bf16 v[80:83], v[120:123], v[132:135], 0
	v_cvt_pk_bf16_f32 v49, v74, v75
	v_cvt_pk_bf16_f32 v72, v76, v77
	v_cvt_pk_bf16_f32 v73, v78, v79
	s_waitcnt lgkmcnt(0)
	v_mfma_f32_16x16x32_bf16 v[74:77], v[136:139], v[140:143], v[80:83]
	v_mfma_f32_16x16x32_bf16 v[38:41], v[104:107], v[46:49], v[38:41]
	v_mfma_f32_16x16x32_bf16 v[42:45], v[108:111], v[46:49], v[42:45]
	s_nop 5
	v_cndmask_b32_e64 v2, v74, v2, s[10:11]
	v_cndmask_b32_e64 v2, v2, v74, s[8:9]
	v_cndmask_b32_e64 v3, 0, v75, s[8:9]
	v_cndmask_b32_e64 v5, v76, 0, s[6:7]
	v_cndmask_b32_e64 v71, v77, 0, vcc
	v_cvt_pk_bf16_f32 v74, v2, v3
	v_cvt_pk_bf16_f32 v75, v5, v71
	v_lshl_add_u64 v[2:3], s[18:19], 0, v[64:65]
	s_nop 0
	v_mfma_f32_16x16x32_bf16 v[38:41], v[54:57], v[72:75], v[38:41]
	s_nop 7
	v_cvt_pk_bf16_f32 v38, v38, v39
	v_cvt_pk_bf16_f32 v39, v40, v41
	global_store_dwordx2 v[2:3], v[38:39], off
	v_mfma_f32_16x16x32_bf16 v[38:41], v[50:53], v[72:75], v[42:45]
	s_nop 7
	v_cvt_pk_bf16_f32 v38, v38, v39
	v_cvt_pk_bf16_f32 v39, v40, v41
	global_store_dwordx2 v[2:3], v[38:39], off offset:32
	s_branch .Lgla_upd
